# diff-attention output epilogue: tile staged through a per-wave 4 KiB LDS area (free V buffer 0) and written with 16-byte stores (16 per wave instead of 128 four-byte stores)
# baseline (speedup 1.0000x reference)
.Lmk_b1e:
	s_waitcnt vmcnt(8)
	s_waitcnt vmcnt(9)
	ds_write_b128 v0, v[194:197]
	s_waitcnt vmcnt(8)
	ds_write_b128 v0, v[198:201] offset:8192
	s_and_saveexec_b64 s[2:3], s[0:1]
	v_add_f32_e32 v0, v222, v223
	v_fmac_f32_e32 v0, v214, v221
	v_add_f32_e32 v158, v216, v217
	v_fmac_f32_e32 v158, v0, v215
	ds_write_b32 v212, v158
	s_or_b64 exec, exec, s[2:3]
	s_waitcnt lgkmcnt(0)
	ds_read_b128 v[190:193], v211
	s_ashr_i32 s65, s64, 31
	ds_read_b128 v[186:189], v211 offset:32
	ds_read_b128 v[182:185], v211 offset:64
	ds_read_b128 v[158:161], v211 offset:96
	s_lshl_b64 s[0:1], s[64:65], 13
	v_readlane_b32 s2, v254, 17
	s_waitcnt lgkmcnt(3)
	v_rcp_f32_e32 v190, v190
	v_readlane_b32 s3, v254, 18
	s_add_u32 s2, s2, s0
	v_and_b32_e32 v0, 1, v233
	s_addc_u32 s3, s3, s1
	v_cmp_eq_u32_e64 s[0:1], 0, v0
	v_lshlrev_b32_e32 v0, 1, v242
	v_lshl_add_u64 v[194:195], s[2:3], 0, v[0:1]
	v_lshlrev_b32_e32 v0, 15, v210
	v_lshl_add_u64 v[194:195], v[194:195], 0, v[0:1]
	s_waitcnt lgkmcnt(0)
	v_rcp_f32_e32 v191, v191
	v_rcp_f32_e32 v192, v192
	v_rcp_f32_e32 v193, v193
	v_rcp_f32_e32 v186, v186
	v_rcp_f32_e32 v187, v187
	v_rcp_f32_e32 v188, v188
	v_rcp_f32_e32 v189, v189
	v_rcp_f32_e32 v182, v182
	v_rcp_f32_e32 v183, v183
	v_rcp_f32_e32 v184, v184
	v_rcp_f32_e32 v185, v185
	v_rcp_f32_e32 v158, v158
	v_rcp_f32_e32 v159, v159
	v_rcp_f32_e32 v160, v160
	v_rcp_f32_e32 v161, v161
	s_nop 1
	v_mul_f32_e32 v114, v114, v190
	v_mul_f32_e32 v98, v98, v190
	v_mul_f32_e32 v82, v82, v190
	v_mul_f32_e32 v66, v66, v190
	v_mul_f32_e32 v50, v50, v190
	v_mul_f32_e32 v34, v34, v190
	v_mul_f32_e32 v18, v18, v190
	v_mul_f32_e32 v2, v2, v190
	v_mul_f32_e32 v115, v115, v191
	v_mul_f32_e32 v99, v99, v191
	v_mul_f32_e32 v83, v83, v191
	v_mul_f32_e32 v67, v67, v191
	v_mul_f32_e32 v51, v51, v191
	v_mul_f32_e32 v35, v35, v191
	v_mul_f32_e32 v19, v19, v191
	v_mul_f32_e32 v3, v3, v191
	v_mul_f32_e32 v116, v116, v192
	v_mul_f32_e32 v100, v100, v192
	v_mul_f32_e32 v84, v84, v192
	v_mul_f32_e32 v68, v68, v192
	v_mul_f32_e32 v52, v52, v192
	v_mul_f32_e32 v36, v36, v192
	v_mul_f32_e32 v20, v20, v192
	v_mul_f32_e32 v4, v4, v192
	v_mul_f32_e32 v117, v117, v193
	v_mul_f32_e32 v101, v101, v193
	v_mul_f32_e32 v85, v85, v193
	v_mul_f32_e32 v69, v69, v193
	v_mul_f32_e32 v53, v53, v193
	v_mul_f32_e32 v37, v37, v193
	v_mul_f32_e32 v21, v21, v193
	v_mul_f32_e32 v5, v5, v193
	v_mul_f32_e32 v118, v118, v186
	v_mul_f32_e32 v102, v102, v186
	v_mul_f32_e32 v86, v86, v186
	v_mul_f32_e32 v70, v70, v186
	v_mul_f32_e32 v54, v54, v186
	v_mul_f32_e32 v38, v38, v186
	v_mul_f32_e32 v22, v22, v186
	v_mul_f32_e32 v6, v6, v186
	v_mul_f32_e32 v119, v119, v187
	v_mul_f32_e32 v103, v103, v187
	v_mul_f32_e32 v87, v87, v187
	v_mul_f32_e32 v71, v71, v187
	v_mul_f32_e32 v55, v55, v187
	v_mul_f32_e32 v39, v39, v187
	v_mul_f32_e32 v23, v23, v187
	v_mul_f32_e32 v7, v7, v187
	v_mul_f32_e32 v120, v120, v188
	v_mul_f32_e32 v104, v104, v188
	v_mul_f32_e32 v88, v88, v188
	v_mul_f32_e32 v72, v72, v188
	v_mul_f32_e32 v56, v56, v188
	v_mul_f32_e32 v40, v40, v188
	v_mul_f32_e32 v24, v24, v188
	v_mul_f32_e32 v8, v8, v188
	v_mul_f32_e32 v121, v121, v189
	v_mul_f32_e32 v105, v105, v189
	v_mul_f32_e32 v89, v89, v189
	v_mul_f32_e32 v73, v73, v189
	v_mul_f32_e32 v57, v57, v189
	v_mul_f32_e32 v41, v41, v189
	v_mul_f32_e32 v25, v25, v189
	v_mul_f32_e32 v9, v9, v189
	v_mul_f32_e32 v122, v122, v182
	v_mul_f32_e32 v106, v106, v182
	v_mul_f32_e32 v90, v90, v182
	v_mul_f32_e32 v74, v74, v182
	v_mul_f32_e32 v58, v58, v182
	v_mul_f32_e32 v42, v42, v182
	v_mul_f32_e32 v26, v26, v182
	v_mul_f32_e32 v10, v10, v182
	v_mul_f32_e32 v123, v123, v183
	v_mul_f32_e32 v107, v107, v183
	v_mul_f32_e32 v91, v91, v183
	v_mul_f32_e32 v75, v75, v183
	v_mul_f32_e32 v59, v59, v183
	v_mul_f32_e32 v43, v43, v183
	v_mul_f32_e32 v27, v27, v183
	v_mul_f32_e32 v11, v11, v183
	v_mul_f32_e32 v124, v124, v184
	v_mul_f32_e32 v108, v108, v184
	v_mul_f32_e32 v92, v92, v184
	v_mul_f32_e32 v76, v76, v184
	v_mul_f32_e32 v60, v60, v184
	v_mul_f32_e32 v44, v44, v184
	v_mul_f32_e32 v28, v28, v184
	v_mul_f32_e32 v12, v12, v184
	v_mul_f32_e32 v125, v125, v185
	v_mul_f32_e32 v109, v109, v185
	v_mul_f32_e32 v93, v93, v185
	v_mul_f32_e32 v77, v77, v185
	v_mul_f32_e32 v61, v61, v185
	v_mul_f32_e32 v45, v45, v185
	v_mul_f32_e32 v29, v29, v185
	v_mul_f32_e32 v13, v13, v185
	v_mul_f32_e32 v126, v126, v158
	v_mul_f32_e32 v110, v110, v158
	v_mul_f32_e32 v94, v94, v158
	v_mul_f32_e32 v78, v78, v158
	v_mul_f32_e32 v62, v62, v158
	v_mul_f32_e32 v46, v46, v158
	v_mul_f32_e32 v30, v30, v158
	v_mul_f32_e32 v14, v14, v158
	v_mul_f32_e32 v127, v127, v159
	v_mul_f32_e32 v111, v111, v159
	v_mul_f32_e32 v95, v95, v159
	v_mul_f32_e32 v79, v79, v159
	v_mul_f32_e32 v63, v63, v159
	v_mul_f32_e32 v47, v47, v159
	v_mul_f32_e32 v31, v31, v159
	v_mul_f32_e32 v15, v15, v159
	v_mul_f32_e32 v128, v128, v160
	v_mul_f32_e32 v112, v112, v160
	v_mul_f32_e32 v96, v96, v160
	v_mul_f32_e32 v80, v80, v160
	v_mul_f32_e32 v64, v64, v160
	v_mul_f32_e32 v48, v48, v160
	v_mul_f32_e32 v32, v32, v160
	v_mul_f32_e32 v16, v16, v160
	v_mul_f32_e32 v129, v129, v161
	v_mul_f32_e32 v113, v113, v161
	v_mul_f32_e32 v97, v97, v161
	v_mul_f32_e32 v81, v81, v161
	v_mul_f32_e32 v65, v65, v161
	v_mul_f32_e32 v49, v49, v161
	v_mul_f32_e32 v33, v33, v161
	v_mul_f32_e32 v17, v17, v161
	s_lshl_b32 s0, s64, 7
	v_lshlrev_b32_e32 v158, 9, v210
	v_lshl_add_u32 v158, v242, 1, v158
	v_add_u32_e32 v158, s0, v158
	v_lshl_add_u32 v159, v233, 4, s0
	v_lshrrev_b32_e32 v160, 3, v233
	v_lshlrev_b32_e32 v160, 13, v160
	v_and_b32_e32 v161, 7, v233
	v_lshl_or_b32 v160, v161, 4, v160
	v_mov_b32_e32 v161, 0
	v_lshl_add_u64 v[182:183], s[2:3], 0, v[160:161]
	s_mov_b64 s[0:1], 0x10000
	v_lshl_add_u64 v[184:185], v[182:183], 0, s[0:1]
	v_lshl_add_u64 v[186:187], v[184:185], 0, s[0:1]
	v_lshl_add_u64 v[188:189], v[186:187], 0, s[0:1]
	v_cvt_pk_bf16_f32 v0, v114, v114
	ds_write_b16 v158, v0
	v_cvt_pk_bf16_f32 v0, v98, v98
	ds_write_b16 v158, v0 offset:64
	v_cvt_pk_bf16_f32 v0, v115, v115
	ds_write_b16 v158, v0 offset:128
	v_cvt_pk_bf16_f32 v0, v99, v99
	ds_write_b16 v158, v0 offset:192
	v_cvt_pk_bf16_f32 v0, v116, v116
	ds_write_b16 v158, v0 offset:256
	v_cvt_pk_bf16_f32 v0, v100, v100
	ds_write_b16 v158, v0 offset:320
	v_cvt_pk_bf16_f32 v0, v117, v117
	ds_write_b16 v158, v0 offset:384
	v_cvt_pk_bf16_f32 v0, v101, v101
	ds_write_b16 v158, v0 offset:448
	v_cvt_pk_bf16_f32 v0, v118, v118
	ds_write_b16 v158, v0 offset:1024
	v_cvt_pk_bf16_f32 v0, v102, v102
	ds_write_b16 v158, v0 offset:1088
	v_cvt_pk_bf16_f32 v0, v119, v119
	ds_write_b16 v158, v0 offset:1152
	v_cvt_pk_bf16_f32 v0, v103, v103
	ds_write_b16 v158, v0 offset:1216
	v_cvt_pk_bf16_f32 v0, v120, v120
	ds_write_b16 v158, v0 offset:1280
	v_cvt_pk_bf16_f32 v0, v104, v104
	ds_write_b16 v158, v0 offset:1344
	v_cvt_pk_bf16_f32 v0, v121, v121
	ds_write_b16 v158, v0 offset:1408
	v_cvt_pk_bf16_f32 v0, v105, v105
	ds_write_b16 v158, v0 offset:1472
	v_cvt_pk_bf16_f32 v0, v122, v122
	ds_write_b16 v158, v0 offset:2048
	v_cvt_pk_bf16_f32 v0, v106, v106
	ds_write_b16 v158, v0 offset:2112
	v_cvt_pk_bf16_f32 v0, v123, v123
	ds_write_b16 v158, v0 offset:2176
	v_cvt_pk_bf16_f32 v0, v107, v107
	ds_write_b16 v158, v0 offset:2240
	v_cvt_pk_bf16_f32 v0, v124, v124
	ds_write_b16 v158, v0 offset:2304
	v_cvt_pk_bf16_f32 v0, v108, v108
	ds_write_b16 v158, v0 offset:2368
	v_cvt_pk_bf16_f32 v0, v125, v125
	ds_write_b16 v158, v0 offset:2432
	v_cvt_pk_bf16_f32 v0, v109, v109
	ds_write_b16 v158, v0 offset:2496
	v_cvt_pk_bf16_f32 v0, v126, v126
	ds_write_b16 v158, v0 offset:3072
	v_cvt_pk_bf16_f32 v0, v110, v110
	ds_write_b16 v158, v0 offset:3136
	v_cvt_pk_bf16_f32 v0, v127, v127
	ds_write_b16 v158, v0 offset:3200
	v_cvt_pk_bf16_f32 v0, v111, v111
	ds_write_b16 v158, v0 offset:3264
	v_cvt_pk_bf16_f32 v0, v128, v128
	ds_write_b16 v158, v0 offset:3328
	v_cvt_pk_bf16_f32 v0, v112, v112
	ds_write_b16 v158, v0 offset:3392
	v_cvt_pk_bf16_f32 v0, v129, v129
	ds_write_b16 v158, v0 offset:3456
	v_cvt_pk_bf16_f32 v0, v113, v113
	ds_write_b16 v158, v0 offset:3520
	ds_read_b128 v[114:117], v159
	ds_read_b128 v[118:121], v159 offset:1024
	ds_read_b128 v[122:125], v159 offset:2048
	ds_read_b128 v[126:129], v159 offset:3072
	s_waitcnt lgkmcnt(0)
	global_store_dwordx4 v[182:183], v[114:117], off
	global_store_dwordx4 v[184:185], v[118:121], off
	global_store_dwordx4 v[186:187], v[122:125], off
	global_store_dwordx4 v[188:189], v[126:129], off
	v_cvt_pk_bf16_f32 v0, v82, v82
	ds_write_b16 v158, v0
	v_cvt_pk_bf16_f32 v0, v66, v66
	ds_write_b16 v158, v0 offset:64
	v_cvt_pk_bf16_f32 v0, v83, v83
	ds_write_b16 v158, v0 offset:128
	v_cvt_pk_bf16_f32 v0, v67, v67
	ds_write_b16 v158, v0 offset:192
	v_cvt_pk_bf16_f32 v0, v84, v84
	ds_write_b16 v158, v0 offset:256
	v_cvt_pk_bf16_f32 v0, v68, v68
	ds_write_b16 v158, v0 offset:320
	v_cvt_pk_bf16_f32 v0, v85, v85
	ds_write_b16 v158, v0 offset:384
	v_cvt_pk_bf16_f32 v0, v69, v69
	ds_write_b16 v158, v0 offset:448
	v_cvt_pk_bf16_f32 v0, v86, v86
	ds_write_b16 v158, v0 offset:1024
	v_cvt_pk_bf16_f32 v0, v70, v70
	ds_write_b16 v158, v0 offset:1088
	v_cvt_pk_bf16_f32 v0, v87, v87
	ds_write_b16 v158, v0 offset:1152
	v_cvt_pk_bf16_f32 v0, v71, v71
	ds_write_b16 v158, v0 offset:1216
	v_cvt_pk_bf16_f32 v0, v88, v88
	ds_write_b16 v158, v0 offset:1280
	v_cvt_pk_bf16_f32 v0, v72, v72
	ds_write_b16 v158, v0 offset:1344
	v_cvt_pk_bf16_f32 v0, v89, v89
	ds_write_b16 v158, v0 offset:1408
	v_cvt_pk_bf16_f32 v0, v73, v73
	ds_write_b16 v158, v0 offset:1472
	v_cvt_pk_bf16_f32 v0, v90, v90
	ds_write_b16 v158, v0 offset:2048
	v_cvt_pk_bf16_f32 v0, v74, v74
	ds_write_b16 v158, v0 offset:2112
	v_cvt_pk_bf16_f32 v0, v91, v91
	ds_write_b16 v158, v0 offset:2176
	v_cvt_pk_bf16_f32 v0, v75, v75
	ds_write_b16 v158, v0 offset:2240
	v_cvt_pk_bf16_f32 v0, v92, v92
	ds_write_b16 v158, v0 offset:2304
	v_cvt_pk_bf16_f32 v0, v76, v76
	ds_write_b16 v158, v0 offset:2368
	v_cvt_pk_bf16_f32 v0, v93, v93
	ds_write_b16 v158, v0 offset:2432
	v_cvt_pk_bf16_f32 v0, v77, v77
	ds_write_b16 v158, v0 offset:2496
	v_cvt_pk_bf16_f32 v0, v94, v94
	ds_write_b16 v158, v0 offset:3072
	v_cvt_pk_bf16_f32 v0, v78, v78
	ds_write_b16 v158, v0 offset:3136
	v_cvt_pk_bf16_f32 v0, v95, v95
	ds_write_b16 v158, v0 offset:3200
	v_cvt_pk_bf16_f32 v0, v79, v79
	ds_write_b16 v158, v0 offset:3264
	v_cvt_pk_bf16_f32 v0, v96, v96
	ds_write_b16 v158, v0 offset:3328
	v_cvt_pk_bf16_f32 v0, v80, v80
	ds_write_b16 v158, v0 offset:3392
	v_cvt_pk_bf16_f32 v0, v97, v97
	ds_write_b16 v158, v0 offset:3456
	v_cvt_pk_bf16_f32 v0, v81, v81
	ds_write_b16 v158, v0 offset:3520
	ds_read_b128 v[82:85], v159
	ds_read_b128 v[86:89], v159 offset:1024
	ds_read_b128 v[90:93], v159 offset:2048
	ds_read_b128 v[94:97], v159 offset:3072
	s_waitcnt lgkmcnt(0)
	global_store_dwordx4 v[182:183], v[82:85], off offset:128
	global_store_dwordx4 v[184:185], v[86:89], off offset:128
	global_store_dwordx4 v[186:187], v[90:93], off offset:128
	global_store_dwordx4 v[188:189], v[94:97], off offset:128
	v_cvt_pk_bf16_f32 v0, v50, v50
	ds_write_b16 v158, v0
	v_cvt_pk_bf16_f32 v0, v34, v34
	ds_write_b16 v158, v0 offset:64
	v_cvt_pk_bf16_f32 v0, v51, v51
	ds_write_b16 v158, v0 offset:128
	v_cvt_pk_bf16_f32 v0, v35, v35
	ds_write_b16 v158, v0 offset:192
	v_cvt_pk_bf16_f32 v0, v52, v52
	ds_write_b16 v158, v0 offset:256
	v_cvt_pk_bf16_f32 v0, v36, v36
	ds_write_b16 v158, v0 offset:320
	v_cvt_pk_bf16_f32 v0, v53, v53
	ds_write_b16 v158, v0 offset:384
	v_cvt_pk_bf16_f32 v0, v37, v37
	ds_write_b16 v158, v0 offset:448
	v_cvt_pk_bf16_f32 v0, v54, v54
	ds_write_b16 v158, v0 offset:1024
	v_cvt_pk_bf16_f32 v0, v38, v38
	ds_write_b16 v158, v0 offset:1088
	v_cvt_pk_bf16_f32 v0, v55, v55
	ds_write_b16 v158, v0 offset:1152
	v_cvt_pk_bf16_f32 v0, v39, v39
	ds_write_b16 v158, v0 offset:1216
	v_cvt_pk_bf16_f32 v0, v56, v56
	ds_write_b16 v158, v0 offset:1280
	v_cvt_pk_bf16_f32 v0, v40, v40
	ds_write_b16 v158, v0 offset:1344
	v_cvt_pk_bf16_f32 v0, v57, v57
	ds_write_b16 v158, v0 offset:1408
	v_cvt_pk_bf16_f32 v0, v41, v41
	ds_write_b16 v158, v0 offset:1472
	v_cvt_pk_bf16_f32 v0, v58, v58
	ds_write_b16 v158, v0 offset:2048
	v_cvt_pk_bf16_f32 v0, v42, v42
	ds_write_b16 v158, v0 offset:2112
	v_cvt_pk_bf16_f32 v0, v59, v59
	ds_write_b16 v158, v0 offset:2176
	v_cvt_pk_bf16_f32 v0, v43, v43
	ds_write_b16 v158, v0 offset:2240
	v_cvt_pk_bf16_f32 v0, v60, v60
	ds_write_b16 v158, v0 offset:2304
	v_cvt_pk_bf16_f32 v0, v44, v44
	ds_write_b16 v158, v0 offset:2368
	v_cvt_pk_bf16_f32 v0, v61, v61
	ds_write_b16 v158, v0 offset:2432
	v_cvt_pk_bf16_f32 v0, v45, v45
	ds_write_b16 v158, v0 offset:2496
	v_cvt_pk_bf16_f32 v0, v62, v62
	ds_write_b16 v158, v0 offset:3072
	v_cvt_pk_bf16_f32 v0, v46, v46
	ds_write_b16 v158, v0 offset:3136
	v_cvt_pk_bf16_f32 v0, v63, v63
	ds_write_b16 v158, v0 offset:3200
	v_cvt_pk_bf16_f32 v0, v47, v47
	ds_write_b16 v158, v0 offset:3264
	v_cvt_pk_bf16_f32 v0, v64, v64
	ds_write_b16 v158, v0 offset:3328
	v_cvt_pk_bf16_f32 v0, v48, v48
	ds_write_b16 v158, v0 offset:3392
	v_cvt_pk_bf16_f32 v0, v65, v65
	ds_write_b16 v158, v0 offset:3456
	v_cvt_pk_bf16_f32 v0, v49, v49
	ds_write_b16 v158, v0 offset:3520
	ds_read_b128 v[50:53], v159
	ds_read_b128 v[54:57], v159 offset:1024
	ds_read_b128 v[58:61], v159 offset:2048
	ds_read_b128 v[62:65], v159 offset:3072
	s_waitcnt lgkmcnt(0)
	global_store_dwordx4 v[182:183], v[50:53], off offset:256
	global_store_dwordx4 v[184:185], v[54:57], off offset:256
	global_store_dwordx4 v[186:187], v[58:61], off offset:256
	global_store_dwordx4 v[188:189], v[62:65], off offset:256
	v_cvt_pk_bf16_f32 v0, v18, v18
	ds_write_b16 v158, v0
	v_cvt_pk_bf16_f32 v0, v2, v2
	ds_write_b16 v158, v0 offset:64
	v_cvt_pk_bf16_f32 v0, v19, v19
	ds_write_b16 v158, v0 offset:128
	v_cvt_pk_bf16_f32 v0, v3, v3
	ds_write_b16 v158, v0 offset:192
	v_cvt_pk_bf16_f32 v0, v20, v20
	ds_write_b16 v158, v0 offset:256
	v_cvt_pk_bf16_f32 v0, v4, v4
	ds_write_b16 v158, v0 offset:320
	v_cvt_pk_bf16_f32 v0, v21, v21
	ds_write_b16 v158, v0 offset:384
	v_cvt_pk_bf16_f32 v0, v5, v5
	ds_write_b16 v158, v0 offset:448
	v_cvt_pk_bf16_f32 v0, v22, v22
	ds_write_b16 v158, v0 offset:1024
	v_cvt_pk_bf16_f32 v0, v6, v6
	ds_write_b16 v158, v0 offset:1088
	v_cvt_pk_bf16_f32 v0, v23, v23
	ds_write_b16 v158, v0 offset:1152
	v_cvt_pk_bf16_f32 v0, v7, v7
	ds_write_b16 v158, v0 offset:1216
	v_cvt_pk_bf16_f32 v0, v24, v24
	ds_write_b16 v158, v0 offset:1280
	v_cvt_pk_bf16_f32 v0, v8, v8
	ds_write_b16 v158, v0 offset:1344
	v_cvt_pk_bf16_f32 v0, v25, v25
	ds_write_b16 v158, v0 offset:1408
	v_cvt_pk_bf16_f32 v0, v9, v9
	ds_write_b16 v158, v0 offset:1472
	v_cvt_pk_bf16_f32 v0, v26, v26
	ds_write_b16 v158, v0 offset:2048
	v_cvt_pk_bf16_f32 v0, v10, v10
	ds_write_b16 v158, v0 offset:2112
	v_cvt_pk_bf16_f32 v0, v27, v27
	ds_write_b16 v158, v0 offset:2176
	v_cvt_pk_bf16_f32 v0, v11, v11
	ds_write_b16 v158, v0 offset:2240
	v_cvt_pk_bf16_f32 v0, v28, v28
	ds_write_b16 v158, v0 offset:2304
	v_cvt_pk_bf16_f32 v0, v12, v12
	ds_write_b16 v158, v0 offset:2368
	v_cvt_pk_bf16_f32 v0, v29, v29
	ds_write_b16 v158, v0 offset:2432
	v_cvt_pk_bf16_f32 v0, v13, v13
	ds_write_b16 v158, v0 offset:2496
	v_cvt_pk_bf16_f32 v0, v30, v30
	ds_write_b16 v158, v0 offset:3072
	v_cvt_pk_bf16_f32 v0, v14, v14
	ds_write_b16 v158, v0 offset:3136
	v_cvt_pk_bf16_f32 v0, v31, v31
	ds_write_b16 v158, v0 offset:3200
	v_cvt_pk_bf16_f32 v0, v15, v15
	ds_write_b16 v158, v0 offset:3264
	v_cvt_pk_bf16_f32 v0, v32, v32
	ds_write_b16 v158, v0 offset:3328
	v_cvt_pk_bf16_f32 v0, v16, v16
	ds_write_b16 v158, v0 offset:3392
	v_cvt_pk_bf16_f32 v0, v33, v33
	ds_write_b16 v158, v0 offset:3456
	v_cvt_pk_bf16_f32 v0, v17, v17
	ds_write_b16 v158, v0 offset:3520
	ds_read_b128 v[18:21], v159
	ds_read_b128 v[22:25], v159 offset:1024
	ds_read_b128 v[26:29], v159 offset:2048
	ds_read_b128 v[30:33], v159 offset:3072
	s_waitcnt lgkmcnt(0)
	global_store_dwordx4 v[182:183], v[18:21], off offset:384
	global_store_dwordx4 v[184:185], v[22:25], off offset:384
	global_store_dwordx4 v[186:187], v[26:29], off offset:384
	global_store_dwordx4 v[188:189], v[30:33], off offset:384
	s_mov_b64 s[2:3], 0
	s_nop 0
	s_branch .LBB0_1348
